# speedup vs baseline: 1.0262x; 1.0059x over previous
.Ltile0:
	s_mov_b32 s34, 0
	s_waitcnt vmcnt(5)
	s_waitcnt lgkmcnt(0)
	s_barrier
	s_mul_i32 s35, s33, 0xa000
	v_add_u32_e32 v240, s35, v222
	v_add_u32_e32 v241, s35, v223
	v_add_u32_e32 v242, s35, v224
	s_add_u32 s33, s33, 1
	s_cmp_eq_u32 s33, 3
	s_cselect_b32 s33, 0, s33
	ds_read_b128 v[244:247], v240 offset:6144
	ds_read_b128 v[252:255], v240 offset:7168
	v_mfma_scale_f32_16x16x128_f8f6f4 v[0:3], v[128:131], v[160:165], 0, v208, v216 op_sel_hi:[0,0,0] cbsz:4 blgp:2
	s_cmp_eq_u32 s34, 13
	s_cselect_b32 s36, s38, s36
	s_cselect_b32 s37, s39, s37
	s_mov_b32 m0, s40
	v_mfma_scale_f32_16x16x128_f8f6f4 v[4:7], v[128:131], v[166:171], 0, v208, v217 op_sel_hi:[0,0,0] cbsz:4 blgp:2
	ds_read_b128 v[184:187], v241 offset:0
	v_mfma_scale_f32_16x16x128_f8f6f4 v[8:11], v[128:131], v[172:177], 0, v208, v218 op_sel_hi:[0,0,0] cbsz:4 blgp:2
	buffer_load_dwordx4 v221, s[4:7], s36 offen lds
	v_mfma_scale_f32_16x16x128_f8f6f4 v[12:15], v[128:131], v[178:183], 0, v208, v219 op_sel_hi:[0,0,0] cbsz:4 blgp:2
	s_add_u32 m0, s40, 0x2000
	ds_read_b64 v[188:189], v242 offset:0
	v_mfma_scale_f32_16x16x128_f8f6f4 v[16:19], v[132:135], v[160:165], 0, v209, v216 op_sel_hi:[0,0,0] cbsz:4 blgp:2
	buffer_load_dwordx4 v225, s[4:7], s36 offen lds
	v_mfma_scale_f32_16x16x128_f8f6f4 v[20:23], v[132:135], v[166:171], 0, v209, v217 op_sel_hi:[0,0,0] cbsz:4 blgp:2
	s_add_u32 m0, s40, 0x4000
	ds_read_b128 v[190:193], v241 offset:1536
	v_mfma_scale_f32_16x16x128_f8f6f4 v[24:27], v[132:135], v[172:177], 0, v209, v218 op_sel_hi:[0,0,0] cbsz:4 blgp:2
	buffer_load_dwordx4 v221, s[4:7], s37 offen lds
	v_mfma_scale_f32_16x16x128_f8f6f4 v[28:31], v[132:135], v[178:183], 0, v209, v219 op_sel_hi:[0,0,0] cbsz:4 blgp:2
	s_add_u32 m0, s40, 0x6000
	ds_read_b64 v[194:195], v242 offset:1536
	v_mfma_scale_f32_16x16x128_f8f6f4 v[32:35], v[136:139], v[160:165], 0, v210, v216 op_sel_hi:[0,0,0] cbsz:4 blgp:2
	buffer_load_dwordx4 v225, s[4:7], s37 offen lds
	v_mfma_scale_f32_16x16x128_f8f6f4 v[36:39], v[136:139], v[166:171], 0, v210, v217 op_sel_hi:[0,0,0] cbsz:4 blgp:2
	s_add_u32 m0, s40, 0x8000
	ds_read_b128 v[196:199], v241 offset:3072
	v_mfma_scale_f32_16x16x128_f8f6f4 v[40:43], v[136:139], v[172:177], 0, v210, v218 op_sel_hi:[0,0,0] cbsz:4 blgp:2
	buffer_load_dwordx4 v226, s[4:7], s37 offen lds
	v_mfma_scale_f32_16x16x128_f8f6f4 v[44:47], v[136:139], v[178:183], 0, v210, v219 op_sel_hi:[0,0,0] cbsz:4 blgp:2
	ds_read_b64 v[200:201], v242 offset:3072
	v_mfma_scale_f32_16x16x128_f8f6f4 v[48:51], v[140:143], v[160:165], 0, v211, v216 op_sel_hi:[0,0,0] cbsz:4 blgp:2
	ds_read_b128 v[202:205], v241 offset:4608
	v_mfma_scale_f32_16x16x128_f8f6f4 v[52:55], v[140:143], v[166:171], 0, v211, v217 op_sel_hi:[0,0,0] cbsz:4 blgp:2
	ds_read_b64 v[206:207], v242 offset:4608
	v_mfma_scale_f32_16x16x128_f8f6f4 v[56:59], v[140:143], v[172:177], 0, v211, v218 op_sel_hi:[0,0,0] cbsz:4 blgp:2
	s_add_u32 s36, s36, 0x4000
	s_add_u32 s37, s37, 0x6000
	s_add_u32 s40, s40, 0xa000
	s_sub_u32 s41, s40, 0x1e000
	v_mfma_scale_f32_16x16x128_f8f6f4 v[60:63], v[140:143], v[178:183], 0, v211, v219 op_sel_hi:[0,0,0] cbsz:4 blgp:2
	s_cmp_ge_u32 s40, s49
	s_cselect_b32 s40, s41, s40
	ds_read_b128 v[128:131], v240 offset:0
	v_mfma_scale_f32_16x16x128_f8f6f4 v[64:67], v[144:147], v[160:165], 0, v212, v216 op_sel_hi:[0,0,0] cbsz:4 blgp:2
	ds_read_b128 v[132:135], v240 offset:1024
	v_mfma_scale_f32_16x16x128_f8f6f4 v[68:71], v[144:147], v[166:171], 0, v212, v217 op_sel_hi:[0,0,0] cbsz:4 blgp:2
	ds_read_b128 v[136:139], v240 offset:2048
	v_mfma_scale_f32_16x16x128_f8f6f4 v[72:75], v[144:147], v[172:177], 0, v212, v218 op_sel_hi:[0,0,0] cbsz:4 blgp:2
	ds_read_b128 v[140:143], v240 offset:3072
	v_mfma_scale_f32_16x16x128_f8f6f4 v[76:79], v[144:147], v[178:183], 0, v212, v219 op_sel_hi:[0,0,0] cbsz:4 blgp:2
	v_mfma_scale_f32_16x16x128_f8f6f4 v[80:83], v[148:151], v[160:165], 0, v213, v216 op_sel_hi:[0,0,0] cbsz:4 blgp:2
	ds_read_b128 v[144:147], v240 offset:4096
	v_mfma_scale_f32_16x16x128_f8f6f4 v[84:87], v[148:151], v[166:171], 0, v213, v217 op_sel_hi:[0,0,0] cbsz:4 blgp:2
	v_mfma_scale_f32_16x16x128_f8f6f4 v[88:91], v[148:151], v[172:177], 0, v213, v218 op_sel_hi:[0,0,0] cbsz:4 blgp:2
	v_mfma_scale_f32_16x16x128_f8f6f4 v[92:95], v[148:151], v[178:183], 0, v213, v219 op_sel_hi:[0,0,0] cbsz:4 blgp:2
	v_mfma_scale_f32_16x16x128_f8f6f4 v[96:99], v[152:155], v[160:165], 0, v214, v216 op_sel_hi:[0,0,0] cbsz:4 blgp:2
	ds_read_b128 v[148:151], v240 offset:5120
	v_mfma_scale_f32_16x16x128_f8f6f4 v[100:103], v[152:155], v[166:171], 0, v214, v217 op_sel_hi:[0,0,0] cbsz:4 blgp:2
	v_mfma_scale_f32_16x16x128_f8f6f4 v[104:107], v[152:155], v[172:177], 0, v214, v218 op_sel_hi:[0,0,0] cbsz:4 blgp:2
	v_mfma_scale_f32_16x16x128_f8f6f4 v[108:111], v[152:155], v[178:183], 0, v214, v219 op_sel_hi:[0,0,0] cbsz:4 blgp:2
	v_mfma_scale_f32_16x16x128_f8f6f4 v[112:115], v[156:159], v[160:165], 0, v215, v216 op_sel_hi:[0,0,0] cbsz:4 blgp:2
	v_mfma_scale_f32_16x16x128_f8f6f4 v[116:119], v[156:159], v[166:171], 0, v215, v217 op_sel_hi:[0,0,0] cbsz:4 blgp:2
	v_mfma_scale_f32_16x16x128_f8f6f4 v[120:123], v[156:159], v[172:177], 0, v215, v218 op_sel_hi:[0,0,0] cbsz:4 blgp:2
	v_mfma_scale_f32_16x16x128_f8f6f4 v[124:127], v[156:159], v[178:183], 0, v215, v219 op_sel_hi:[0,0,0] cbsz:4 blgp:2
	s_add_u32 s34, s34, 1
	s_waitcnt vmcnt(5)
	s_waitcnt lgkmcnt(0)
	s_barrier
	s_mul_i32 s35, s33, 0xa000
	v_add_u32_e32 v240, s35, v222
	v_add_u32_e32 v241, s35, v223
	v_add_u32_e32 v242, s35, v224
	s_add_u32 s33, s33, 1
	s_cmp_eq_u32 s33, 3
	s_cselect_b32 s33, 0, s33
	ds_read_b128 v[152:155], v240 offset:6144
	ds_read_b128 v[156:159], v240 offset:7168
	v_mfma_scale_f32_16x16x128_f8f6f4 v[0:3], v[128:131], v[184:189], v[0:3], v208, v216 op_sel_hi:[0,0,0] cbsz:4 blgp:2
	s_cmp_eq_u32 s34, 13
	s_cselect_b32 s36, s38, s36
	s_cselect_b32 s37, s39, s37
	s_mov_b32 m0, s40
	v_mfma_scale_f32_16x16x128_f8f6f4 v[4:7], v[128:131], v[190:195], v[4:7], v208, v217 op_sel_hi:[0,0,0] cbsz:4 blgp:2
	ds_read_b128 v[160:163], v241 offset:0
	v_mfma_scale_f32_16x16x128_f8f6f4 v[8:11], v[128:131], v[196:201], v[8:11], v208, v218 op_sel_hi:[0,0,0] cbsz:4 blgp:2
	buffer_load_dwordx4 v221, s[4:7], s36 offen lds
	v_mfma_scale_f32_16x16x128_f8f6f4 v[12:15], v[128:131], v[202:207], v[12:15], v208, v219 op_sel_hi:[0,0,0] cbsz:4 blgp:2
	s_add_u32 m0, s40, 0x2000
	ds_read_b64 v[164:165], v242 offset:0
	v_mfma_scale_f32_16x16x128_f8f6f4 v[16:19], v[132:135], v[184:189], v[16:19], v209, v216 op_sel_hi:[0,0,0] cbsz:4 blgp:2
	buffer_load_dwordx4 v225, s[4:7], s36 offen lds
	v_mfma_scale_f32_16x16x128_f8f6f4 v[20:23], v[132:135], v[190:195], v[20:23], v209, v217 op_sel_hi:[0,0,0] cbsz:4 blgp:2
	s_add_u32 m0, s40, 0x4000
	ds_read_b128 v[166:169], v241 offset:1536
	v_mfma_scale_f32_16x16x128_f8f6f4 v[24:27], v[132:135], v[196:201], v[24:27], v209, v218 op_sel_hi:[0,0,0] cbsz:4 blgp:2
	buffer_load_dwordx4 v221, s[4:7], s37 offen lds
	v_mfma_scale_f32_16x16x128_f8f6f4 v[28:31], v[132:135], v[202:207], v[28:31], v209, v219 op_sel_hi:[0,0,0] cbsz:4 blgp:2
	s_add_u32 m0, s40, 0x6000
	ds_read_b64 v[170:171], v242 offset:1536
	v_mfma_scale_f32_16x16x128_f8f6f4 v[32:35], v[136:139], v[184:189], v[32:35], v210, v216 op_sel_hi:[0,0,0] cbsz:4 blgp:2
	buffer_load_dwordx4 v225, s[4:7], s37 offen lds
	v_mfma_scale_f32_16x16x128_f8f6f4 v[36:39], v[136:139], v[190:195], v[36:39], v210, v217 op_sel_hi:[0,0,0] cbsz:4 blgp:2
	s_add_u32 m0, s40, 0x8000
	ds_read_b128 v[172:175], v241 offset:3072
	v_mfma_scale_f32_16x16x128_f8f6f4 v[40:43], v[136:139], v[196:201], v[40:43], v210, v218 op_sel_hi:[0,0,0] cbsz:4 blgp:2
	buffer_load_dwordx4 v226, s[4:7], s37 offen lds
	v_mfma_scale_f32_16x16x128_f8f6f4 v[44:47], v[136:139], v[202:207], v[44:47], v210, v219 op_sel_hi:[0,0,0] cbsz:4 blgp:2
	ds_read_b64 v[176:177], v242 offset:3072
	v_mfma_scale_f32_16x16x128_f8f6f4 v[48:51], v[140:143], v[184:189], v[48:51], v211, v216 op_sel_hi:[0,0,0] cbsz:4 blgp:2
	ds_read_b128 v[178:181], v241 offset:4608
	v_mfma_scale_f32_16x16x128_f8f6f4 v[52:55], v[140:143], v[190:195], v[52:55], v211, v217 op_sel_hi:[0,0,0] cbsz:4 blgp:2
	ds_read_b64 v[182:183], v242 offset:4608
	v_mfma_scale_f32_16x16x128_f8f6f4 v[56:59], v[140:143], v[196:201], v[56:59], v211, v218 op_sel_hi:[0,0,0] cbsz:4 blgp:2
	s_add_u32 s36, s36, 0x4000
	s_add_u32 s37, s37, 0x6000
	s_add_u32 s40, s40, 0xa000
	s_sub_u32 s41, s40, 0x1e000
	v_mfma_scale_f32_16x16x128_f8f6f4 v[60:63], v[140:143], v[202:207], v[60:63], v211, v219 op_sel_hi:[0,0,0] cbsz:4 blgp:2
	s_cmp_ge_u32 s40, s49
	s_cselect_b32 s40, s41, s40
	ds_read_b128 v[128:131], v240 offset:0
	v_mfma_scale_f32_16x16x128_f8f6f4 v[64:67], v[144:147], v[184:189], v[64:67], v212, v216 op_sel_hi:[0,0,0] cbsz:4 blgp:2
	ds_read_b128 v[132:135], v240 offset:1024
	v_mfma_scale_f32_16x16x128_f8f6f4 v[68:71], v[144:147], v[190:195], v[68:71], v212, v217 op_sel_hi:[0,0,0] cbsz:4 blgp:2
	ds_read_b128 v[136:139], v240 offset:2048
	v_mfma_scale_f32_16x16x128_f8f6f4 v[72:75], v[144:147], v[196:201], v[72:75], v212, v218 op_sel_hi:[0,0,0] cbsz:4 blgp:2
	ds_read_b128 v[140:143], v240 offset:3072
	v_mfma_scale_f32_16x16x128_f8f6f4 v[76:79], v[144:147], v[202:207], v[76:79], v212, v219 op_sel_hi:[0,0,0] cbsz:4 blgp:2
	v_mfma_scale_f32_16x16x128_f8f6f4 v[80:83], v[148:151], v[184:189], v[80:83], v213, v216 op_sel_hi:[0,0,0] cbsz:4 blgp:2
	ds_read_b128 v[144:147], v240 offset:4096
	v_mfma_scale_f32_16x16x128_f8f6f4 v[84:87], v[148:151], v[190:195], v[84:87], v213, v217 op_sel_hi:[0,0,0] cbsz:4 blgp:2
	v_mfma_scale_f32_16x16x128_f8f6f4 v[88:91], v[148:151], v[196:201], v[88:91], v213, v218 op_sel_hi:[0,0,0] cbsz:4 blgp:2
	v_mfma_scale_f32_16x16x128_f8f6f4 v[92:95], v[148:151], v[202:207], v[92:95], v213, v219 op_sel_hi:[0,0,0] cbsz:4 blgp:2
	v_mfma_scale_f32_16x16x128_f8f6f4 v[96:99], v[244:247], v[184:189], v[96:99], v214, v216 op_sel_hi:[0,0,0] cbsz:4 blgp:2
	ds_read_b128 v[148:151], v240 offset:5120
	v_mfma_scale_f32_16x16x128_f8f6f4 v[100:103], v[244:247], v[190:195], v[100:103], v214, v217 op_sel_hi:[0,0,0] cbsz:4 blgp:2
	v_mfma_scale_f32_16x16x128_f8f6f4 v[104:107], v[244:247], v[196:201], v[104:107], v214, v218 op_sel_hi:[0,0,0] cbsz:4 blgp:2
	v_mfma_scale_f32_16x16x128_f8f6f4 v[108:111], v[244:247], v[202:207], v[108:111], v214, v219 op_sel_hi:[0,0,0] cbsz:4 blgp:2
	v_mfma_scale_f32_16x16x128_f8f6f4 v[112:115], v[252:255], v[184:189], v[112:115], v215, v216 op_sel_hi:[0,0,0] cbsz:4 blgp:2
	v_mfma_scale_f32_16x16x128_f8f6f4 v[116:119], v[252:255], v[190:195], v[116:119], v215, v217 op_sel_hi:[0,0,0] cbsz:4 blgp:2
	v_mfma_scale_f32_16x16x128_f8f6f4 v[120:123], v[252:255], v[196:201], v[120:123], v215, v218 op_sel_hi:[0,0,0] cbsz:4 blgp:2
	v_mfma_scale_f32_16x16x128_f8f6f4 v[124:127], v[252:255], v[202:207], v[124:127], v215, v219 op_sel_hi:[0,0,0] cbsz:4 blgp:2
	s_add_u32 s34, s34, 1
.Lkloop0:
	s_waitcnt vmcnt(5)
	s_waitcnt lgkmcnt(0)
	s_barrier
	s_mul_i32 s35, s33, 0xa000
	v_add_u32_e32 v240, s35, v222
	v_add_u32_e32 v241, s35, v223
	v_add_u32_e32 v242, s35, v224
	s_add_u32 s33, s33, 1
	s_cmp_eq_u32 s33, 3
	s_cselect_b32 s33, 0, s33
	ds_read_b128 v[244:247], v240 offset:6144
	ds_read_b128 v[252:255], v240 offset:7168
	v_mfma_scale_f32_16x16x128_f8f6f4 v[0:3], v[128:131], v[160:165], v[0:3], v208, v216 op_sel_hi:[0,0,0] cbsz:4 blgp:2
	s_cmp_eq_u32 s34, 13
	s_cselect_b32 s36, s38, s36
	s_cselect_b32 s37, s39, s37
	s_mov_b32 m0, s40
	v_mfma_scale_f32_16x16x128_f8f6f4 v[4:7], v[128:131], v[166:171], v[4:7], v208, v217 op_sel_hi:[0,0,0] cbsz:4 blgp:2
	ds_read_b128 v[184:187], v241 offset:0
	v_mfma_scale_f32_16x16x128_f8f6f4 v[8:11], v[128:131], v[172:177], v[8:11], v208, v218 op_sel_hi:[0,0,0] cbsz:4 blgp:2
	buffer_load_dwordx4 v221, s[4:7], s36 offen lds
	v_mfma_scale_f32_16x16x128_f8f6f4 v[12:15], v[128:131], v[178:183], v[12:15], v208, v219 op_sel_hi:[0,0,0] cbsz:4 blgp:2
	s_add_u32 m0, s40, 0x2000
	ds_read_b64 v[188:189], v242 offset:0
	v_mfma_scale_f32_16x16x128_f8f6f4 v[16:19], v[132:135], v[160:165], v[16:19], v209, v216 op_sel_hi:[0,0,0] cbsz:4 blgp:2
	buffer_load_dwordx4 v225, s[4:7], s36 offen lds
	v_mfma_scale_f32_16x16x128_f8f6f4 v[20:23], v[132:135], v[166:171], v[20:23], v209, v217 op_sel_hi:[0,0,0] cbsz:4 blgp:2
	s_add_u32 m0, s40, 0x4000
	ds_read_b128 v[190:193], v241 offset:1536
	v_mfma_scale_f32_16x16x128_f8f6f4 v[24:27], v[132:135], v[172:177], v[24:27], v209, v218 op_sel_hi:[0,0,0] cbsz:4 blgp:2
	buffer_load_dwordx4 v221, s[4:7], s37 offen lds
	v_mfma_scale_f32_16x16x128_f8f6f4 v[28:31], v[132:135], v[178:183], v[28:31], v209, v219 op_sel_hi:[0,0,0] cbsz:4 blgp:2
	s_add_u32 m0, s40, 0x6000
	ds_read_b64 v[194:195], v242 offset:1536
	v_mfma_scale_f32_16x16x128_f8f6f4 v[32:35], v[136:139], v[160:165], v[32:35], v210, v216 op_sel_hi:[0,0,0] cbsz:4 blgp:2
	buffer_load_dwordx4 v225, s[4:7], s37 offen lds
	v_mfma_scale_f32_16x16x128_f8f6f4 v[36:39], v[136:139], v[166:171], v[36:39], v210, v217 op_sel_hi:[0,0,0] cbsz:4 blgp:2
	s_add_u32 m0, s40, 0x8000
	ds_read_b128 v[196:199], v241 offset:3072
	v_mfma_scale_f32_16x16x128_f8f6f4 v[40:43], v[136:139], v[172:177], v[40:43], v210, v218 op_sel_hi:[0,0,0] cbsz:4 blgp:2
	buffer_load_dwordx4 v226, s[4:7], s37 offen lds
	v_mfma_scale_f32_16x16x128_f8f6f4 v[44:47], v[136:139], v[178:183], v[44:47], v210, v219 op_sel_hi:[0,0,0] cbsz:4 blgp:2
	ds_read_b64 v[200:201], v242 offset:3072
	v_mfma_scale_f32_16x16x128_f8f6f4 v[48:51], v[140:143], v[160:165], v[48:51], v211, v216 op_sel_hi:[0,0,0] cbsz:4 blgp:2
	ds_read_b128 v[202:205], v241 offset:4608
	v_mfma_scale_f32_16x16x128_f8f6f4 v[52:55], v[140:143], v[166:171], v[52:55], v211, v217 op_sel_hi:[0,0,0] cbsz:4 blgp:2
	ds_read_b64 v[206:207], v242 offset:4608
	v_mfma_scale_f32_16x16x128_f8f6f4 v[56:59], v[140:143], v[172:177], v[56:59], v211, v218 op_sel_hi:[0,0,0] cbsz:4 blgp:2
	s_add_u32 s36, s36, 0x4000
	s_add_u32 s37, s37, 0x6000
	s_add_u32 s40, s40, 0xa000
	s_sub_u32 s41, s40, 0x1e000
	v_mfma_scale_f32_16x16x128_f8f6f4 v[60:63], v[140:143], v[178:183], v[60:63], v211, v219 op_sel_hi:[0,0,0] cbsz:4 blgp:2
	s_cmp_ge_u32 s40, s49
	s_cselect_b32 s40, s41, s40
	ds_read_b128 v[128:131], v240 offset:0
	v_mfma_scale_f32_16x16x128_f8f6f4 v[64:67], v[144:147], v[160:165], v[64:67], v212, v216 op_sel_hi:[0,0,0] cbsz:4 blgp:2
	ds_read_b128 v[132:135], v240 offset:1024
	v_mfma_scale_f32_16x16x128_f8f6f4 v[68:71], v[144:147], v[166:171], v[68:71], v212, v217 op_sel_hi:[0,0,0] cbsz:4 blgp:2
	ds_read_b128 v[136:139], v240 offset:2048
	v_mfma_scale_f32_16x16x128_f8f6f4 v[72:75], v[144:147], v[172:177], v[72:75], v212, v218 op_sel_hi:[0,0,0] cbsz:4 blgp:2
	ds_read_b128 v[140:143], v240 offset:3072
	v_mfma_scale_f32_16x16x128_f8f6f4 v[76:79], v[144:147], v[178:183], v[76:79], v212, v219 op_sel_hi:[0,0,0] cbsz:4 blgp:2
	v_mfma_scale_f32_16x16x128_f8f6f4 v[80:83], v[148:151], v[160:165], v[80:83], v213, v216 op_sel_hi:[0,0,0] cbsz:4 blgp:2
	ds_read_b128 v[144:147], v240 offset:4096
	v_mfma_scale_f32_16x16x128_f8f6f4 v[84:87], v[148:151], v[166:171], v[84:87], v213, v217 op_sel_hi:[0,0,0] cbsz:4 blgp:2
	v_mfma_scale_f32_16x16x128_f8f6f4 v[88:91], v[148:151], v[172:177], v[88:91], v213, v218 op_sel_hi:[0,0,0] cbsz:4 blgp:2
	v_mfma_scale_f32_16x16x128_f8f6f4 v[92:95], v[148:151], v[178:183], v[92:95], v213, v219 op_sel_hi:[0,0,0] cbsz:4 blgp:2
	v_mfma_scale_f32_16x16x128_f8f6f4 v[96:99], v[152:155], v[160:165], v[96:99], v214, v216 op_sel_hi:[0,0,0] cbsz:4 blgp:2
	ds_read_b128 v[148:151], v240 offset:5120
	v_mfma_scale_f32_16x16x128_f8f6f4 v[100:103], v[152:155], v[166:171], v[100:103], v214, v217 op_sel_hi:[0,0,0] cbsz:4 blgp:2
	v_mfma_scale_f32_16x16x128_f8f6f4 v[104:107], v[152:155], v[172:177], v[104:107], v214, v218 op_sel_hi:[0,0,0] cbsz:4 blgp:2
	v_mfma_scale_f32_16x16x128_f8f6f4 v[108:111], v[152:155], v[178:183], v[108:111], v214, v219 op_sel_hi:[0,0,0] cbsz:4 blgp:2
	v_mfma_scale_f32_16x16x128_f8f6f4 v[112:115], v[156:159], v[160:165], v[112:115], v215, v216 op_sel_hi:[0,0,0] cbsz:4 blgp:2
	v_mfma_scale_f32_16x16x128_f8f6f4 v[116:119], v[156:159], v[166:171], v[116:119], v215, v217 op_sel_hi:[0,0,0] cbsz:4 blgp:2
	v_mfma_scale_f32_16x16x128_f8f6f4 v[120:123], v[156:159], v[172:177], v[120:123], v215, v218 op_sel_hi:[0,0,0] cbsz:4 blgp:2
	v_mfma_scale_f32_16x16x128_f8f6f4 v[124:127], v[156:159], v[178:183], v[124:127], v215, v219 op_sel_hi:[0,0,0] cbsz:4 blgp:2
	s_add_u32 s34, s34, 1
	s_waitcnt vmcnt(5)
	s_waitcnt lgkmcnt(0)
	s_barrier
	s_mul_i32 s35, s33, 0xa000
	v_add_u32_e32 v240, s35, v222
	v_add_u32_e32 v241, s35, v223
	v_add_u32_e32 v242, s35, v224
	s_add_u32 s33, s33, 1
	s_cmp_eq_u32 s33, 3
	s_cselect_b32 s33, 0, s33
	ds_read_b128 v[152:155], v240 offset:6144
	ds_read_b128 v[156:159], v240 offset:7168
	v_mfma_scale_f32_16x16x128_f8f6f4 v[0:3], v[128:131], v[184:189], v[0:3], v208, v216 op_sel_hi:[0,0,0] cbsz:4 blgp:2
	s_cmp_eq_u32 s34, 13
	s_cselect_b32 s36, s38, s36
	s_cselect_b32 s37, s39, s37
	s_mov_b32 m0, s40
	v_mfma_scale_f32_16x16x128_f8f6f4 v[4:7], v[128:131], v[190:195], v[4:7], v208, v217 op_sel_hi:[0,0,0] cbsz:4 blgp:2
	ds_read_b128 v[160:163], v241 offset:0
	v_mfma_scale_f32_16x16x128_f8f6f4 v[8:11], v[128:131], v[196:201], v[8:11], v208, v218 op_sel_hi:[0,0,0] cbsz:4 blgp:2
	buffer_load_dwordx4 v221, s[4:7], s36 offen lds
	v_mfma_scale_f32_16x16x128_f8f6f4 v[12:15], v[128:131], v[202:207], v[12:15], v208, v219 op_sel_hi:[0,0,0] cbsz:4 blgp:2
	s_add_u32 m0, s40, 0x2000
	ds_read_b64 v[164:165], v242 offset:0
	v_mfma_scale_f32_16x16x128_f8f6f4 v[16:19], v[132:135], v[184:189], v[16:19], v209, v216 op_sel_hi:[0,0,0] cbsz:4 blgp:2
	buffer_load_dwordx4 v225, s[4:7], s36 offen lds
	v_mfma_scale_f32_16x16x128_f8f6f4 v[20:23], v[132:135], v[190:195], v[20:23], v209, v217 op_sel_hi:[0,0,0] cbsz:4 blgp:2
	s_add_u32 m0, s40, 0x4000
	ds_read_b128 v[166:169], v241 offset:1536
	v_mfma_scale_f32_16x16x128_f8f6f4 v[24:27], v[132:135], v[196:201], v[24:27], v209, v218 op_sel_hi:[0,0,0] cbsz:4 blgp:2
	buffer_load_dwordx4 v221, s[4:7], s37 offen lds
	v_mfma_scale_f32_16x16x128_f8f6f4 v[28:31], v[132:135], v[202:207], v[28:31], v209, v219 op_sel_hi:[0,0,0] cbsz:4 blgp:2
	s_add_u32 m0, s40, 0x6000
	ds_read_b64 v[170:171], v242 offset:1536
	v_mfma_scale_f32_16x16x128_f8f6f4 v[32:35], v[136:139], v[184:189], v[32:35], v210, v216 op_sel_hi:[0,0,0] cbsz:4 blgp:2
	buffer_load_dwordx4 v225, s[4:7], s37 offen lds
	v_mfma_scale_f32_16x16x128_f8f6f4 v[36:39], v[136:139], v[190:195], v[36:39], v210, v217 op_sel_hi:[0,0,0] cbsz:4 blgp:2
	s_add_u32 m0, s40, 0x8000
	ds_read_b128 v[172:175], v241 offset:3072
	v_mfma_scale_f32_16x16x128_f8f6f4 v[40:43], v[136:139], v[196:201], v[40:43], v210, v218 op_sel_hi:[0,0,0] cbsz:4 blgp:2
	buffer_load_dwordx4 v226, s[4:7], s37 offen lds
	v_mfma_scale_f32_16x16x128_f8f6f4 v[44:47], v[136:139], v[202:207], v[44:47], v210, v219 op_sel_hi:[0,0,0] cbsz:4 blgp:2
	ds_read_b64 v[176:177], v242 offset:3072
	v_mfma_scale_f32_16x16x128_f8f6f4 v[48:51], v[140:143], v[184:189], v[48:51], v211, v216 op_sel_hi:[0,0,0] cbsz:4 blgp:2
	ds_read_b128 v[178:181], v241 offset:4608
	v_mfma_scale_f32_16x16x128_f8f6f4 v[52:55], v[140:143], v[190:195], v[52:55], v211, v217 op_sel_hi:[0,0,0] cbsz:4 blgp:2
	ds_read_b64 v[182:183], v242 offset:4608
	v_mfma_scale_f32_16x16x128_f8f6f4 v[56:59], v[140:143], v[196:201], v[56:59], v211, v218 op_sel_hi:[0,0,0] cbsz:4 blgp:2
	s_add_u32 s36, s36, 0x4000
	s_add_u32 s37, s37, 0x6000
	s_add_u32 s40, s40, 0xa000
	s_sub_u32 s41, s40, 0x1e000
	v_mfma_scale_f32_16x16x128_f8f6f4 v[60:63], v[140:143], v[202:207], v[60:63], v211, v219 op_sel_hi:[0,0,0] cbsz:4 blgp:2
	s_cmp_ge_u32 s40, s49
	s_cselect_b32 s40, s41, s40
	ds_read_b128 v[128:131], v240 offset:0
	v_mfma_scale_f32_16x16x128_f8f6f4 v[64:67], v[144:147], v[184:189], v[64:67], v212, v216 op_sel_hi:[0,0,0] cbsz:4 blgp:2
	ds_read_b128 v[132:135], v240 offset:1024
	v_mfma_scale_f32_16x16x128_f8f6f4 v[68:71], v[144:147], v[190:195], v[68:71], v212, v217 op_sel_hi:[0,0,0] cbsz:4 blgp:2
	ds_read_b128 v[136:139], v240 offset:2048
	v_mfma_scale_f32_16x16x128_f8f6f4 v[72:75], v[144:147], v[196:201], v[72:75], v212, v218 op_sel_hi:[0,0,0] cbsz:4 blgp:2
	ds_read_b128 v[140:143], v240 offset:3072
	v_mfma_scale_f32_16x16x128_f8f6f4 v[76:79], v[144:147], v[202:207], v[76:79], v212, v219 op_sel_hi:[0,0,0] cbsz:4 blgp:2
	v_mfma_scale_f32_16x16x128_f8f6f4 v[80:83], v[148:151], v[184:189], v[80:83], v213, v216 op_sel_hi:[0,0,0] cbsz:4 blgp:2
	ds_read_b128 v[144:147], v240 offset:4096
	v_mfma_scale_f32_16x16x128_f8f6f4 v[84:87], v[148:151], v[190:195], v[84:87], v213, v217 op_sel_hi:[0,0,0] cbsz:4 blgp:2
	v_mfma_scale_f32_16x16x128_f8f6f4 v[88:91], v[148:151], v[196:201], v[88:91], v213, v218 op_sel_hi:[0,0,0] cbsz:4 blgp:2
	v_mfma_scale_f32_16x16x128_f8f6f4 v[92:95], v[148:151], v[202:207], v[92:95], v213, v219 op_sel_hi:[0,0,0] cbsz:4 blgp:2
	v_mfma_scale_f32_16x16x128_f8f6f4 v[96:99], v[244:247], v[184:189], v[96:99], v214, v216 op_sel_hi:[0,0,0] cbsz:4 blgp:2
	ds_read_b128 v[148:151], v240 offset:5120
	v_mfma_scale_f32_16x16x128_f8f6f4 v[100:103], v[244:247], v[190:195], v[100:103], v214, v217 op_sel_hi:[0,0,0] cbsz:4 blgp:2
	v_mfma_scale_f32_16x16x128_f8f6f4 v[104:107], v[244:247], v[196:201], v[104:107], v214, v218 op_sel_hi:[0,0,0] cbsz:4 blgp:2
	v_mfma_scale_f32_16x16x128_f8f6f4 v[108:111], v[244:247], v[202:207], v[108:111], v214, v219 op_sel_hi:[0,0,0] cbsz:4 blgp:2
	v_mfma_scale_f32_16x16x128_f8f6f4 v[112:115], v[252:255], v[184:189], v[112:115], v215, v216 op_sel_hi:[0,0,0] cbsz:4 blgp:2
	v_mfma_scale_f32_16x16x128_f8f6f4 v[116:119], v[252:255], v[190:195], v[116:119], v215, v217 op_sel_hi:[0,0,0] cbsz:4 blgp:2
	v_mfma_scale_f32_16x16x128_f8f6f4 v[120:123], v[252:255], v[196:201], v[120:123], v215, v218 op_sel_hi:[0,0,0] cbsz:4 blgp:2
	v_mfma_scale_f32_16x16x128_f8f6f4 v[124:127], v[252:255], v[202:207], v[124:127], v215, v219 op_sel_hi:[0,0,0] cbsz:4 blgp:2
	s_cmp_eq_u32 s34, 13
	s_cbranch_scc0 .Lnosc_or0
	s_add_u32 s44, s23, 1
	s_and_b32 s44, s44, 1
	s_cmp_lt_u32 s18, 4
	s_cselect_b32 s80, s26, s27
	s_cselect_b32 s82, s8, s10
	s_cselect_b32 s83, s9, s11
	s_lshl_b32 s80, s80, 10
	s_and_b32 s84, s18, 3
	s_lshl_b32 s84, s84, 8
	s_add_u32 s80, s80, s84
	s_add_u32 s82, s82, s80
	s_addc_u32 s83, s83, 0
	s_lshl_b32 s84, s44, 11
	s_lshl_b32 s85, s18, 8
	s_add_u32 s84, s84, s85
	s_add_u32 s84, s84, 0x1e000
	s_mov_b32 m0, s84
	v_lshlrev_b32_e32 v236, 2, v220
	global_load_lds_dword v236, s[82:83]
